# GQA loop: cross-half combine of the softmax row sums deferred to the loop exit (per-lane partial sums in the loop)
# baseline (speedup 1.0000x reference)
; #define SBAR() __builtin_amdgcn_sched_barrier(0)
; __device__ __forceinline__ void finishSM(f32x16& p0, f32x16& p1, float alpha, float& l_reg, bf16x8& pa0, bf16x8& pa1, bf16x8& pa2, bf16x8& pa3) {
; #pragma unroll
;     for (int r = 0; r < 16; ++r) p1[r] = EXP_PROBE ? fmaf(p1[r], 0.001f, 1.f) : __builtin_amdgcn_exp2f(p1[r]);
;     float ps = 0.f;
; #pragma unroll
;     for (int r = 0; r < 16; ++r) ps += p0[r];
; #pragma unroll
;     for (int r = 0; r < 16; ++r) ps += p1[r];
;     { auto rr = __builtin_amdgcn_permlane32_swap(__float_as_uint(ps), __float_as_uint(ps), false, false);
;       ps = __uint_as_float(rr[0]) + __uint_as_float(rr[1]); }
;     l_reg = l_reg * alpha + ps;
;     ATT_PKN(p0, 0, pa0); ATT_PKN(p0, 8, pa1); ATT_PKN(p1, 0, pa2); ATT_PKN(p1, 8, pa3);
; }
; template <bool FIXM> __device__ __forceinline__ void pv_psm(f32x16& o0, f32x16& o1, unsigned vb, bf16x8 pa0, bf16x8 pa1, bf16x8 pa2, bf16x8 pa3,
;                                        f32x16& p0, f32x16& p1, float& m_reg, f32x16& negm, float& alpha) {
;     { const s16x4 l0 = tr_read<v_rd_off(0, 0, 0)>(vb), h0 = tr_read<v_rd_off(0, 0, 1)>(vb), l1 = tr_read<v_rd_off(0, 1, 0)>(vb), h1 = tr_read<v_rd_off(0, 1, 1)>(vb);
;       const s16x4 l2 = tr_read<v_rd_off(0, 2, 0)>(vb), h2 = tr_read<v_rd_off(0, 2, 1)>(vb), l3 = tr_read<v_rd_off(0, 3, 0)>(vb), h3 = tr_read<v_rd_off(0, 3, 1)>(vb);
;       float pmax = 0.f; SBAR(); if (!FIXM) pmax = psm_max(p0, p1); else { _Pragma("unroll") for (int r = 0; r < 8; ++r) p0[r] = __builtin_amdgcn_exp2f(p0[r]); } SBAR();
;       asm volatile("s_waitcnt lgkmcnt(0)" ::: "memory"); SBAR();
;       o0 = __builtin_amdgcn_mfma_f32_32x32x16_bf16(ATT_PK(l0, h0), pa0, o0, 0, 0, 0);
;       o0 = __builtin_amdgcn_mfma_f32_32x32x16_bf16(ATT_PK(l1, h1), pa1, o0, 0, 0, 0);
;       o0 = __builtin_amdgcn_mfma_f32_32x32x16_bf16(ATT_PK(l2, h2), pa2, o0, 0, 0, 0);
;       o0 = __builtin_amdgcn_mfma_f32_32x32x16_bf16(ATT_PK(l3, h3), pa3, o0, 0, 0, 0);
;       SBAR();
;       const s16x4 m0 = tr_read<v_rd_off(1, 0, 0)>(vb), n0 = tr_read<v_rd_off(1, 0, 1)>(vb), m1 = tr_read<v_rd_off(1, 1, 0)>(vb), n1 = tr_read<v_rd_off(1, 1, 1)>(vb);
;       const s16x4 m2 = tr_read<v_rd_off(1, 2, 0)>(vb), n2 = tr_read<v_rd_off(1, 2, 1)>(vb), m3 = tr_read<v_rd_off(1, 3, 0)>(vb), n3 = tr_read<v_rd_off(1, 3, 1)>(vb);
.LBB0_497:
	s_waitcnt lgkmcnt(0)
	s_barrier
	ds_read_b128 v[224:227], v223 offset:20480
	ds_read_b128 v[228:231], v223 offset:24576
	ds_read_b128 v[232:235], v252 offset:20480
	ds_read_b128 v[236:239], v252 offset:24576
	ds_read_b128 v[240:243], v253 offset:20480
	ds_read_b128 v[244:247], v253 offset:24576
	ds_read_b128 v[248:251], v2 offset:20480
	v_exp_f32_e32 v66, v66
	v_exp_f32_e32 v67, v67
	v_exp_f32_e32 v68, v68
	v_exp_f32_e32 v69, v69
	v_exp_f32_e32 v70, v70
	v_exp_f32_e32 v71, v71
	v_exp_f32_e32 v72, v72
	v_exp_f32_e32 v73, v73
	s_waitcnt lgkmcnt(6)
	v_mfma_f32_32x32x16_bf16 v[98:113], v[224:227], v[114:117], v[18:33]
	ds_read_b128 v[224:227], v2 offset:24576
	v_exp_f32_e32 v74, v74
	v_exp_f32_e32 v75, v75
	v_exp_f32_e32 v76, v76
	v_cvt_pk_bf16_f32 v156, v143, v145
	v_cvt_pk_bf16_f32 v157, v141, v144
	v_add_f32_e32 v164, v143, v145
	v_add_f32_e32 v164, v141, v164
	s_waitcnt lgkmcnt(6)
	v_mfma_f32_32x32x16_bf16 v[82:97], v[228:231], v[114:117], v[18:33]
	v_exp_f32_e32 v77, v77
	v_exp_f32_e32 v78, v78
	v_exp_f32_e32 v79, v79
	v_cvt_pk_bf16_f32 v158, v139, v142
	v_cvt_pk_bf16_f32 v159, v138, v140
	v_add_f32_e32 v164, v144, v164
	v_add_f32_e32 v164, v139, v164
	v_add_f32_e32 v164, v142, v164
	s_waitcnt lgkmcnt(5)
	v_mfma_f32_32x32x16_bf16 v[98:113], v[232:235], v[12:15], v[98:113]
	v_exp_f32_e32 v80, v80
	v_exp_f32_e32 v81, v81
	v_cvt_pk_bf16_f32 v160, v151, v153
	v_cvt_pk_bf16_f32 v161, v149, v152
	v_cvt_pk_bf16_f32 v162, v147, v150
	v_cvt_pk_bf16_f32 v163, v146, v148
	v_add_f32_e32 v164, v138, v164
	v_add_f32_e32 v164, v140, v164
	v_add_f32_e32 v164, v151, v164
	s_waitcnt lgkmcnt(4)
	v_mfma_f32_32x32x16_bf16 v[82:97], v[236:239], v[12:15], v[82:97]
	v_add_f32_e32 v164, v153, v164
	v_add_f32_e32 v164, v149, v164
	v_add_f32_e32 v164, v152, v164
	v_add_f32_e32 v164, v147, v164
	v_add_f32_e32 v164, v150, v164
	v_add_f32_e32 v164, v146, v164
	v_add_f32_e32 v164, v148, v164
	s_waitcnt lgkmcnt(3)
	v_mfma_f32_32x32x16_bf16 v[98:113], v[240:243], v[8:11], v[98:113]
	ds_read_b64_tr_b16 v[138:139], v213 offset:0
	ds_read_b64_tr_b16 v[140:141], v213 offset:1024
	ds_read_b64_tr_b16 v[142:143], v213 offset:2048
	ds_read_b64_tr_b16 v[144:145], v213 offset:3072
	v_add_f32_e32 v164, v66, v164
	v_add_f32_e32 v164, v67, v164
	v_add_f32_e32 v164, v68, v164
	v_add_f32_e32 v164, v69, v164
	s_waitcnt lgkmcnt(6)
	v_mfma_f32_32x32x16_bf16 v[82:97], v[244:247], v[8:11], v[82:97]
	ds_read_b64_tr_b16 v[146:147], v213 offset:4096
	ds_read_b64_tr_b16 v[148:149], v213 offset:5120
	ds_read_b64_tr_b16 v[150:151], v213 offset:6144
	ds_read_b64_tr_b16 v[152:153], v213 offset:7168
	v_add_f32_e32 v164, v70, v164
	v_add_f32_e32 v164, v71, v164
	v_add_f32_e32 v164, v72, v164
	v_add_f32_e32 v164, v73, v164
	s_waitcnt lgkmcnt(9)
	v_mfma_f32_32x32x16_bf16 v[98:113], v[248:251], v[4:7], v[98:113]
	v_add_f32_e32 v164, v74, v164
	v_add_f32_e32 v164, v75, v164
	v_add_f32_e32 v164, v76, v164
	v_add_f32_e32 v164, v77, v164
	s_waitcnt lgkmcnt(8)
	v_mfma_f32_32x32x16_bf16 v[82:97], v[224:227], v[4:7], v[82:97]
	ds_read_b64_tr_b16 v[224:225], v213 offset:512
	ds_read_b64_tr_b16 v[226:227], v213 offset:1536
	ds_read_b64_tr_b16 v[228:229], v213 offset:2560
	ds_read_b64_tr_b16 v[230:231], v213 offset:3584
	ds_read_b64_tr_b16 v[232:233], v213 offset:4608
	ds_read_b64_tr_b16 v[234:235], v213 offset:5632
	ds_read_b64_tr_b16 v[236:237], v213 offset:6656
	ds_read_b64_tr_b16 v[238:239], v213 offset:7680
	s_waitcnt lgkmcnt(8)
	v_mfma_f32_32x32x16_bf16 v[50:65], v[138:141], v[156:159], v[50:65]
	v_add_f32_e32 v164, v78, v164
	v_add_f32_e32 v164, v79, v164
	v_add_f32_e32 v164, v80, v164
	v_add_f32_e32 v154, v81, v164
	v_mfma_f32_32x32x16_bf16 v[50:65], v[142:145], v[160:163], v[50:65]
	v_cvt_pk_bf16_f32 v66, v66, v67
	v_cvt_pk_bf16_f32 v67, v68, v69
	v_cvt_pk_bf16_f32 v68, v70, v71
	v_cvt_pk_bf16_f32 v69, v72, v73
	v_cvt_pk_bf16_f32 v70, v74, v75
	v_cvt_pk_bf16_f32 v71, v76, v77
	v_cvt_pk_bf16_f32 v72, v78, v79
	v_cvt_pk_bf16_f32 v73, v80, v81
	v_mfma_f32_32x32x16_bf16 v[50:65], v[146:149], v[66:69], v[50:65]
	s_add_i32 s8, s13, -1
	s_cmp_lt_u32 s8, s31
	s_cselect_b32 s9, 0, s31
	s_cselect_b32 s35, s12, s29
	s_lshl_b32 s9, s9, 6
	s_sub_i32 s9, s35, s9
	s_lshl_b32 s52, s9, 8
	s_add_i32 s52, s52, -16384
	v_mfma_f32_32x32x16_bf16 v[50:65], v[150:153], v[70:73], v[50:65]
	v_add_u32_e32 v126, s52, v137
	global_load_dwordx4 v[130:133], v126, s[42:43]
	global_load_dwordx4 v[126:129], v126, s[44:45]
	s_waitcnt lgkmcnt(0)
	v_mfma_f32_32x32x16_bf16 v[34:49], v[224:227], v[156:159], v[34:49]
	s_waitcnt vmcnt(2)
	ds_write_b128 v187, v[118:121] offset:40960
	ds_write_b128 v214, v[122:125] offset:53248
	v_exp_f32_e32 v168, v98
	v_exp_f32_e32 v169, v99
	v_mfma_f32_32x32x16_bf16 v[34:49], v[228:231], v[160:163], v[34:49]
	v_exp_f32_e32 v170, v100
	v_exp_f32_e32 v171, v101
	v_exp_f32_e32 v172, v102
	v_exp_f32_e32 v173, v103
	v_mfma_f32_32x32x16_bf16 v[34:49], v[232:235], v[66:69], v[34:49]
	v_exp_f32_e32 v174, v104
	v_exp_f32_e32 v175, v105
	v_exp_f32_e32 v176, v106
	v_exp_f32_e32 v177, v107
	v_exp_f32_e32 v178, v108
	v_mfma_f32_32x32x16_bf16 v[34:49], v[236:239], v[70:73], v[34:49]
	v_exp_f32_e32 v179, v109
	v_exp_f32_e32 v180, v110
	v_exp_f32_e32 v181, v111
	v_exp_f32_e32 v182, v112
	v_exp_f32_e32 v183, v113
	s_waitcnt lgkmcnt(0)
	s_barrier
; #define LAS __attribute__((address_space(3)))
; __device__ __forceinline__ void finishSM(f32x16& p0, f32x16& p1, float alpha, float& l_reg, bf16x8& pa0, bf16x8& pa1, bf16x8& pa2, bf16x8& pa3) {
; #pragma unroll
;     for (int r = 0; r < 16; ++r) p1[r] = EXP_PROBE ? fmaf(p1[r], 0.001f, 1.f) : __builtin_amdgcn_exp2f(p1[r]);
;     float ps = 0.f;
; #pragma unroll
;     for (int r = 0; r < 16; ++r) ps += p0[r];
; #pragma unroll
;     for (int r = 0; r < 16; ++r) ps += p1[r];
;     { auto rr = __builtin_amdgcn_permlane32_swap(__float_as_uint(ps), __float_as_uint(ps), false, false);
;       ps = __uint_as_float(rr[0]) + __uint_as_float(rr[1]); }
;     l_reg = l_reg * alpha + ps;
;     ATT_PKN(p0, 0, pa0); ATT_PKN(p0, 8, pa1); ATT_PKN(p1, 0, pa2); ATT_PKN(p1, 8, pa3);
; }
; template <int DQK> __device__ __forceinline__ void qkt(f32x16& p0, f32x16& p1, const LAS char* buf, const bf16x8* qr, int r32, int hi, const f32x16& negm) {
; #pragma unroll
;     for (int d0 = 0; d0 < 4; ++d0) { const int ch = d0 * 2 + hi;
;         const bf16x8 b0 = *(const LAS bf16x8*)(buf + B_KN + swz64(r32, ch));
;         const bf16x8 b1 = *(const LAS bf16x8*)(buf + B_KN + swz64(32 + r32, ch));
;         p0 = __builtin_amdgcn_mfma_f32_32x32x16_bf16(b0, qr[d0], d0 == 0 ? negm : p0, 0, 0, 0);
;         p1 = __builtin_amdgcn_mfma_f32_32x32x16_bf16(b1, qr[d0], d0 == 0 ? negm : p1, 0, 0, 0); }
; template <bool FIXM> __device__ __forceinline__ void pv_psm(f32x16& o0, f32x16& o1, unsigned vb, bf16x8 pa0, bf16x8 pa1, bf16x8 pa2, bf16x8 pa3,
;                                        f32x16& p0, f32x16& p1, float& m_reg, f32x16& negm, float& alpha) {
;     { const s16x4 l0 = tr_read<v_rd_off(0, 0, 0)>(vb), h0 = tr_read<v_rd_off(0, 0, 1)>(vb), l1 = tr_read<v_rd_off(0, 1, 0)>(vb), h1 = tr_read<v_rd_off(0, 1, 1)>(vb);
;       const s16x4 l2 = tr_read<v_rd_off(0, 2, 0)>(vb), h2 = tr_read<v_rd_off(0, 2, 1)>(vb), l3 = tr_read<v_rd_off(0, 3, 0)>(vb), h3 = tr_read<v_rd_off(0, 3, 1)>(vb);
;       float pmax = 0.f; SBAR(); if (!FIXM) pmax = psm_max(p0, p1); else { _Pragma("unroll") for (int r = 0; r < 8; ++r) p0[r] = __builtin_amdgcn_exp2f(p0[r]); } SBAR();
;       asm volatile("s_waitcnt lgkmcnt(0)" ::: "memory"); SBAR();
;       o0 = __builtin_amdgcn_mfma_f32_32x32x16_bf16(ATT_PK(l0, h0), pa0, o0, 0, 0, 0);
;       o0 = __builtin_amdgcn_mfma_f32_32x32x16_bf16(ATT_PK(l1, h1), pa1, o0, 0, 0, 0);
	ds_read_b128 v[224:227], v223 offset:40960
	ds_read_b128 v[228:231], v223 offset:45056
	ds_read_b128 v[232:235], v252 offset:40960
	ds_read_b128 v[236:239], v252 offset:45056
	ds_read_b128 v[240:243], v253 offset:40960
	ds_read_b128 v[244:247], v253 offset:45056
	ds_read_b128 v[248:251], v2 offset:40960
	v_exp_f32_e32 v82, v82
	v_exp_f32_e32 v83, v83
	v_exp_f32_e32 v84, v84
	v_exp_f32_e32 v85, v85
	v_exp_f32_e32 v86, v86
	v_exp_f32_e32 v87, v87
	v_exp_f32_e32 v88, v88
	v_exp_f32_e32 v89, v89
	s_waitcnt lgkmcnt(6)
	v_mfma_f32_32x32x16_bf16 v[98:113], v[224:227], v[114:117], v[18:33]
	ds_read_b128 v[224:227], v2 offset:45056
	v_exp_f32_e32 v90, v90
	v_exp_f32_e32 v91, v91
	v_exp_f32_e32 v92, v92
	v_cvt_pk_bf16_f32 v156, v168, v169
	v_cvt_pk_bf16_f32 v157, v170, v171
	v_add_f32_e32 v164, v168, v169
	v_add_f32_e32 v164, v170, v164
	s_waitcnt lgkmcnt(6)
	v_mfma_f32_32x32x16_bf16 v[66:81], v[228:231], v[114:117], v[18:33]
	v_exp_f32_e32 v93, v93
	v_exp_f32_e32 v94, v94
	v_exp_f32_e32 v95, v95
	v_cvt_pk_bf16_f32 v158, v172, v173
	v_cvt_pk_bf16_f32 v159, v174, v175
	v_add_f32_e32 v164, v171, v164
	v_add_f32_e32 v164, v172, v164
	v_add_f32_e32 v164, v173, v164
	s_waitcnt lgkmcnt(5)
	v_mfma_f32_32x32x16_bf16 v[98:113], v[232:235], v[12:15], v[98:113]
	v_exp_f32_e32 v96, v96
	v_exp_f32_e32 v97, v97
	v_cvt_pk_bf16_f32 v160, v176, v177
	v_cvt_pk_bf16_f32 v161, v178, v179
	v_cvt_pk_bf16_f32 v162, v180, v181
	v_cvt_pk_bf16_f32 v163, v182, v183
	v_add_f32_e32 v164, v174, v164
	v_add_f32_e32 v164, v175, v164
	v_add_f32_e32 v164, v176, v164
	s_waitcnt lgkmcnt(4)
	v_mfma_f32_32x32x16_bf16 v[66:81], v[236:239], v[12:15], v[66:81]
	v_add_f32_e32 v164, v177, v164
	v_add_f32_e32 v164, v178, v164
	v_add_f32_e32 v164, v179, v164
	v_add_f32_e32 v164, v180, v164
	v_add_f32_e32 v164, v181, v164
	v_add_f32_e32 v164, v182, v164
	v_add_f32_e32 v164, v183, v164
	s_waitcnt lgkmcnt(3)
	v_mfma_f32_32x32x16_bf16 v[98:113], v[240:243], v[8:11], v[98:113]
	ds_read_b64_tr_b16 v[168:169], v213 offset:20480
	ds_read_b64_tr_b16 v[170:171], v213 offset:21504
	ds_read_b64_tr_b16 v[172:173], v213 offset:22528
	ds_read_b64_tr_b16 v[174:175], v213 offset:23552
	v_add_f32_e32 v164, v82, v164
	v_add_f32_e32 v164, v83, v164
	v_add_f32_e32 v164, v84, v164
	v_add_f32_e32 v164, v85, v164
	s_waitcnt lgkmcnt(6)
	v_mfma_f32_32x32x16_bf16 v[66:81], v[244:247], v[8:11], v[66:81]
	ds_read_b64_tr_b16 v[176:177], v213 offset:24576
	ds_read_b64_tr_b16 v[178:179], v213 offset:25600
	ds_read_b64_tr_b16 v[180:181], v213 offset:26624
	ds_read_b64_tr_b16 v[182:183], v213 offset:27648
	v_add_f32_e32 v164, v86, v164
	v_add_f32_e32 v164, v87, v164
	v_add_f32_e32 v164, v88, v164
	v_add_f32_e32 v164, v89, v164
	s_waitcnt lgkmcnt(9)
	v_mfma_f32_32x32x16_bf16 v[98:113], v[248:251], v[4:7], v[98:113]
	v_add_f32_e32 v164, v90, v164
	v_add_f32_e32 v164, v91, v164
	v_add_f32_e32 v164, v92, v164
	v_add_f32_e32 v164, v93, v164
	s_waitcnt lgkmcnt(8)
	v_mfma_f32_32x32x16_bf16 v[66:81], v[224:227], v[4:7], v[66:81]
	ds_read_b64_tr_b16 v[224:225], v213 offset:20992
	ds_read_b64_tr_b16 v[226:227], v213 offset:22016
	ds_read_b64_tr_b16 v[228:229], v213 offset:23040
	ds_read_b64_tr_b16 v[230:231], v213 offset:24064
	ds_read_b64_tr_b16 v[232:233], v213 offset:25088
	ds_read_b64_tr_b16 v[234:235], v213 offset:26112
	ds_read_b64_tr_b16 v[236:237], v213 offset:27136
	ds_read_b64_tr_b16 v[238:239], v213 offset:28160
	s_waitcnt lgkmcnt(8)
	v_mfma_f32_32x32x16_bf16 v[50:65], v[168:171], v[156:159], v[50:65]
	v_add_f32_e32 v164, v94, v164
	v_add_f32_e32 v164, v95, v164
	v_add_f32_e32 v164, v96, v164
	v_add_f32_e32 v164, v97, v164
	v_mfma_f32_32x32x16_bf16 v[50:65], v[172:175], v[160:163], v[50:65]
	v_cvt_pk_bf16_f32 v82, v82, v83
	v_cvt_pk_bf16_f32 v83, v84, v85
	v_cvt_pk_bf16_f32 v84, v86, v87
	v_cvt_pk_bf16_f32 v85, v88, v89
	v_cvt_pk_bf16_f32 v86, v90, v91
	v_cvt_pk_bf16_f32 v87, v92, v93
	v_cvt_pk_bf16_f32 v88, v94, v95
	v_cvt_pk_bf16_f32 v89, v96, v97
	v_mfma_f32_32x32x16_bf16 v[50:65], v[176:179], v[82:85], v[50:65]
	v_mfma_f32_32x32x16_bf16 v[50:65], v[180:183], v[86:89], v[50:65]
	s_cmp_ge_u32 s13, s30
	s_cbranch_scc1 .Lgqa_b_noload_0
	s_cmp_lt_u32 s13, s31
	s_cselect_b32 s9, 0, s31
	s_cselect_b32 s35, s12, s29
	s_lshl_b32 s9, s9, 6
	s_sub_i32 s9, s35, s9
	s_lshl_b32 s52, s9, 8
	v_add_u32_e32 v122, s52, v137
	global_load_dwordx4 v[118:121], v122, s[42:43]
	global_load_dwordx4 v[122:125], v122, s[44:45]
; #define SBAR() __builtin_amdgcn_sched_barrier(0)
; __device__ __forceinline__ void finishSM(f32x16& p0, f32x16& p1, float alpha, float& l_reg, bf16x8& pa0, bf16x8& pa1, bf16x8& pa2, bf16x8& pa3) {
; #pragma unroll
; template <bool FIXM> __device__ __forceinline__ void pv_psm(f32x16& o0, f32x16& o1, unsigned vb, bf16x8 pa0, bf16x8 pa1, bf16x8 pa2, bf16x8 pa3,
;                                        f32x16& p0, f32x16& p1, float& m_reg, f32x16& negm, float& alpha) {
;     { const s16x4 l0 = tr_read<v_rd_off(0, 0, 0)>(vb), h0 = tr_read<v_rd_off(0, 0, 1)>(vb), l1 = tr_read<v_rd_off(0, 1, 0)>(vb), h1 = tr_read<v_rd_off(0, 1, 1)>(vb);
;       const s16x4 l2 = tr_read<v_rd_off(0, 2, 0)>(vb), h2 = tr_read<v_rd_off(0, 2, 1)>(vb), l3 = tr_read<v_rd_off(0, 3, 0)>(vb), h3 = tr_read<v_rd_off(0, 3, 1)>(vb);
;       float pmax = 0.f; SBAR(); if (!FIXM) pmax = psm_max(p0, p1); else { _Pragma("unroll") for (int r = 0; r < 8; ++r) p0[r] = __builtin_amdgcn_exp2f(p0[r]); } SBAR();
;       asm volatile("s_waitcnt lgkmcnt(0)" ::: "memory"); SBAR();
;       o0 = __builtin_amdgcn_mfma_f32_32x32x16_bf16(ATT_PK(l0, h0), pa0, o0, 0, 0, 0);
;       o0 = __builtin_amdgcn_mfma_f32_32x32x16_bf16(ATT_PK(l1, h1), pa1, o0, 0, 0, 0);
;       o0 = __builtin_amdgcn_mfma_f32_32x32x16_bf16(ATT_PK(l2, h2), pa2, o0, 0, 0, 0);
;       o0 = __builtin_amdgcn_mfma_f32_32x32x16_bf16(ATT_PK(l3, h3), pa3, o0, 0, 0, 0);
;       SBAR();
;       const s16x4 m0 = tr_read<v_rd_off(1, 0, 0)>(vb), n0 = tr_read<v_rd_off(1, 0, 1)>(vb), m1 = tr_read<v_rd_off(1, 1, 0)>(vb), n1 = tr_read<v_rd_off(1, 1, 1)>(vb);
;       const s16x4 m2 = tr_read<v_rd_off(1, 2, 0)>(vb), n2 = tr_read<v_rd_off(1, 2, 1)>(vb), m3 = tr_read<v_rd_off(1, 3, 0)>(vb), n3 = tr_read<v_rd_off(1, 3, 1)>(vb);
;       SBAR(); if (!FIXM) psm_apply<false>(p0, p1, pmax, m_reg, negm, alpha); else { alpha = 1.f; _Pragma("unroll") for (int r = 8; r < 16; ++r) p0[r] = __builtin_amdgcn_exp2f(p0[r]); } SBAR();
;       asm volatile("s_waitcnt lgkmcnt(0)" ::: "memory"); SBAR();
;       o1 = __builtin_amdgcn_mfma_f32_32x32x16_bf16(ATT_PK(m0, n0), pa0, o1, 0, 0, 0);
;       o1 = __builtin_amdgcn_mfma_f32_32x32x16_bf16(ATT_PK(m1, n1), pa1, o1, 0, 0, 0);
;       o1 = __builtin_amdgcn_mfma_f32_32x32x16_bf16(ATT_PK(m2, n2), pa2, o1, 0, 0, 0);
;       o1 = __builtin_amdgcn_mfma_f32_32x32x16_bf16(ATT_PK(m3, n3), pa3, o1, 0, 0, 0); }
; }
.Lgqa_b_ld_done_0:
	s_waitcnt lgkmcnt(0)
	v_mfma_f32_32x32x16_bf16 v[34:49], v[224:227], v[156:159], v[34:49]
	s_waitcnt vmcnt(2)
	ds_write_b128 v187, v[130:133] offset:0
	ds_write_b128 v214, v[126:129] offset:12288
	v_exp_f32_e32 v143, v98
	v_exp_f32_e32 v145, v99
	v_mfma_f32_32x32x16_bf16 v[34:49], v[228:231], v[160:163], v[34:49]
	v_exp_f32_e32 v141, v100
	v_exp_f32_e32 v144, v101
	v_exp_f32_e32 v139, v102
	v_exp_f32_e32 v142, v103
	v_mfma_f32_32x32x16_bf16 v[34:49], v[232:235], v[82:85], v[34:49]
	v_exp_f32_e32 v138, v104
	v_exp_f32_e32 v140, v105
	v_exp_f32_e32 v151, v106
	v_exp_f32_e32 v153, v107
	v_exp_f32_e32 v149, v108
	v_mfma_f32_32x32x16_bf16 v[34:49], v[236:239], v[86:89], v[34:49]
	v_exp_f32_e32 v152, v109
	v_exp_f32_e32 v147, v110
	v_exp_f32_e32 v150, v111
	v_exp_f32_e32 v146, v112
	v_exp_f32_e32 v148, v113
	v_add_f32_e32 v136, v136, v154
	v_add_f32_e32 v136, v136, v164
	s_add_i32 s13, s13, 2
	v_add_u32_e32 v137, 0x8000, v137
	s_cmp_lt_u32 s8, s0
	s_cbranch_scc0 .Lgqa_exit_0
	s_waitcnt lgkmcnt(0)
	s_barrier
	ds_read_b128 v[224:227], v223 offset:0
	ds_read_b128 v[228:231], v223 offset:4096
	ds_read_b128 v[232:235], v252 offset:0
	ds_read_b128 v[236:239], v252 offset:4096
	ds_read_b128 v[240:243], v253 offset:0
	ds_read_b128 v[244:247], v253 offset:4096
	ds_read_b128 v[248:251], v2 offset:0
	v_exp_f32_e32 v66, v66
	v_exp_f32_e32 v67, v67
	v_exp_f32_e32 v68, v68
	v_exp_f32_e32 v69, v69
	v_exp_f32_e32 v70, v70
	v_exp_f32_e32 v71, v71
	v_exp_f32_e32 v72, v72
	v_exp_f32_e32 v73, v73
	s_waitcnt lgkmcnt(6)
	v_mfma_f32_32x32x16_bf16 v[98:113], v[224:227], v[114:117], v[18:33]
	ds_read_b128 v[224:227], v2 offset:4096
	v_exp_f32_e32 v74, v74
	v_exp_f32_e32 v75, v75
	v_exp_f32_e32 v76, v76
	v_cvt_pk_bf16_f32 v156, v143, v145
	v_cvt_pk_bf16_f32 v157, v141, v144
	v_add_f32_e32 v164, v143, v145
	v_add_f32_e32 v164, v141, v164
	s_waitcnt lgkmcnt(6)
	v_mfma_f32_32x32x16_bf16 v[82:97], v[228:231], v[114:117], v[18:33]
	v_exp_f32_e32 v77, v77
	v_exp_f32_e32 v78, v78
	v_exp_f32_e32 v79, v79
	v_cvt_pk_bf16_f32 v158, v139, v142
	v_cvt_pk_bf16_f32 v159, v138, v140
	v_add_f32_e32 v164, v144, v164
	v_add_f32_e32 v164, v139, v164
	v_add_f32_e32 v164, v142, v164
	s_waitcnt lgkmcnt(5)
	v_mfma_f32_32x32x16_bf16 v[98:113], v[232:235], v[12:15], v[98:113]
	v_exp_f32_e32 v80, v80
	v_exp_f32_e32 v81, v81
	v_cvt_pk_bf16_f32 v160, v151, v153
	v_cvt_pk_bf16_f32 v161, v149, v152
	v_cvt_pk_bf16_f32 v162, v147, v150
	v_cvt_pk_bf16_f32 v163, v146, v148
	v_add_f32_e32 v164, v138, v164
	v_add_f32_e32 v164, v140, v164
	v_add_f32_e32 v164, v151, v164
	s_waitcnt lgkmcnt(4)
	v_mfma_f32_32x32x16_bf16 v[82:97], v[236:239], v[12:15], v[82:97]
	v_add_f32_e32 v164, v153, v164
	v_add_f32_e32 v164, v149, v164
	v_add_f32_e32 v164, v152, v164
	v_add_f32_e32 v164, v147, v164
	v_add_f32_e32 v164, v150, v164
	v_add_f32_e32 v164, v146, v164
	v_add_f32_e32 v164, v148, v164
	s_waitcnt lgkmcnt(3)
	v_mfma_f32_32x32x16_bf16 v[98:113], v[240:243], v[8:11], v[98:113]
	ds_read_b64_tr_b16 v[138:139], v213 offset:40960
	ds_read_b64_tr_b16 v[140:141], v213 offset:41984
	ds_read_b64_tr_b16 v[142:143], v213 offset:43008
	ds_read_b64_tr_b16 v[144:145], v213 offset:44032
	v_add_f32_e32 v164, v66, v164
	v_add_f32_e32 v164, v67, v164
	v_add_f32_e32 v164, v68, v164
	v_add_f32_e32 v164, v69, v164
	s_waitcnt lgkmcnt(6)
	v_mfma_f32_32x32x16_bf16 v[82:97], v[244:247], v[8:11], v[82:97]
	ds_read_b64_tr_b16 v[146:147], v213 offset:45056
	ds_read_b64_tr_b16 v[148:149], v213 offset:46080
	ds_read_b64_tr_b16 v[150:151], v213 offset:47104
	ds_read_b64_tr_b16 v[152:153], v213 offset:48128
	v_add_f32_e32 v164, v70, v164
	v_add_f32_e32 v164, v71, v164
	v_add_f32_e32 v164, v72, v164
	v_add_f32_e32 v164, v73, v164
	s_waitcnt lgkmcnt(9)
	v_mfma_f32_32x32x16_bf16 v[98:113], v[248:251], v[4:7], v[98:113]
	v_add_f32_e32 v164, v74, v164
	v_add_f32_e32 v164, v75, v164
	v_add_f32_e32 v164, v76, v164
	v_add_f32_e32 v164, v77, v164
	s_waitcnt lgkmcnt(8)
	v_mfma_f32_32x32x16_bf16 v[82:97], v[224:227], v[4:7], v[82:97]
	ds_read_b64_tr_b16 v[224:225], v213 offset:41472
	ds_read_b64_tr_b16 v[226:227], v213 offset:42496
	ds_read_b64_tr_b16 v[228:229], v213 offset:43520
	ds_read_b64_tr_b16 v[230:231], v213 offset:44544
	ds_read_b64_tr_b16 v[232:233], v213 offset:45568
	ds_read_b64_tr_b16 v[234:235], v213 offset:46592
	ds_read_b64_tr_b16 v[236:237], v213 offset:47616
	ds_read_b64_tr_b16 v[238:239], v213 offset:48640
	s_waitcnt lgkmcnt(8)
	v_mfma_f32_32x32x16_bf16 v[50:65], v[138:141], v[156:159], v[50:65]
	v_add_f32_e32 v164, v78, v164
	v_add_f32_e32 v164, v79, v164
	v_add_f32_e32 v164, v80, v164
	v_add_f32_e32 v154, v81, v164
	v_mfma_f32_32x32x16_bf16 v[50:65], v[142:145], v[160:163], v[50:65]
	v_cvt_pk_bf16_f32 v66, v66, v67
	v_cvt_pk_bf16_f32 v67, v68, v69
	v_cvt_pk_bf16_f32 v68, v70, v71
	v_cvt_pk_bf16_f32 v69, v72, v73
	v_cvt_pk_bf16_f32 v70, v74, v75
	v_cvt_pk_bf16_f32 v71, v76, v77
	v_cvt_pk_bf16_f32 v72, v78, v79
	v_cvt_pk_bf16_f32 v73, v80, v81
	v_mfma_f32_32x32x16_bf16 v[50:65], v[146:149], v[66:69], v[50:65]
	s_add_i32 s8, s13, -1
	s_cmp_lt_u32 s8, s31
	s_cselect_b32 s9, 0, s31
	s_cselect_b32 s35, s12, s29
	s_lshl_b32 s9, s9, 6
	s_sub_i32 s9, s35, s9
	s_lshl_b32 s52, s9, 8
	s_add_i32 s52, s52, -16384
	v_mfma_f32_32x32x16_bf16 v[50:65], v[150:153], v[70:73], v[50:65]
	v_add_u32_e32 v126, s52, v137
	global_load_dwordx4 v[130:133], v126, s[42:43]
	global_load_dwordx4 v[126:129], v126, s[44:45]
	s_waitcnt lgkmcnt(0)
	v_mfma_f32_32x32x16_bf16 v[34:49], v[224:227], v[156:159], v[34:49]
	s_waitcnt vmcnt(2)
	ds_write_b128 v187, v[118:121] offset:20480
	ds_write_b128 v214, v[122:125] offset:32768
	v_exp_f32_e32 v168, v98
	v_exp_f32_e32 v169, v99
	v_mfma_f32_32x32x16_bf16 v[34:49], v[228:231], v[160:163], v[34:49]
	v_exp_f32_e32 v170, v100
	v_exp_f32_e32 v171, v101
	v_exp_f32_e32 v172, v102
	v_exp_f32_e32 v173, v103
	v_mfma_f32_32x32x16_bf16 v[34:49], v[232:235], v[66:69], v[34:49]
	v_exp_f32_e32 v174, v104
	v_exp_f32_e32 v175, v105
	v_exp_f32_e32 v176, v106
	v_exp_f32_e32 v177, v107
	v_exp_f32_e32 v178, v108
	v_mfma_f32_32x32x16_bf16 v[34:49], v[236:239], v[70:73], v[34:49]
	v_exp_f32_e32 v179, v109
	v_exp_f32_e32 v180, v110
	v_exp_f32_e32 v181, v111
	v_exp_f32_e32 v182, v112
	v_exp_f32_e32 v183, v113
	s_waitcnt lgkmcnt(0)
	s_barrier
; #define LAS __attribute__((address_space(3)))
; __device__ __forceinline__ void finishSM(f32x16& p0, f32x16& p1, float alpha, float& l_reg, bf16x8& pa0, bf16x8& pa1, bf16x8& pa2, bf16x8& pa3) {
; #pragma unroll
;     for (int r = 0; r < 16; ++r) p1[r] = EXP_PROBE ? fmaf(p1[r], 0.001f, 1.f) : __builtin_amdgcn_exp2f(p1[r]);
;     float ps = 0.f;
; #pragma unroll
;     for (int r = 0; r < 16; ++r) ps += p0[r];
; #pragma unroll
;     for (int r = 0; r < 16; ++r) ps += p1[r];
;     { auto rr = __builtin_amdgcn_permlane32_swap(__float_as_uint(ps), __float_as_uint(ps), false, false);
;       ps = __uint_as_float(rr[0]) + __uint_as_float(rr[1]); }
;     l_reg = l_reg * alpha + ps;
;     ATT_PKN(p0, 0, pa0); ATT_PKN(p0, 8, pa1); ATT_PKN(p1, 0, pa2); ATT_PKN(p1, 8, pa3);
; }
; template <int DQK> __device__ __forceinline__ void qkt(f32x16& p0, f32x16& p1, const LAS char* buf, const bf16x8* qr, int r32, int hi, const f32x16& negm) {
; #pragma unroll
;     for (int d0 = 0; d0 < 4; ++d0) { const int ch = d0 * 2 + hi;
;         const bf16x8 b0 = *(const LAS bf16x8*)(buf + B_KN + swz64(r32, ch));
;         const bf16x8 b1 = *(const LAS bf16x8*)(buf + B_KN + swz64(32 + r32, ch));
;         p0 = __builtin_amdgcn_mfma_f32_32x32x16_bf16(b0, qr[d0], d0 == 0 ? negm : p0, 0, 0, 0);
;         p1 = __builtin_amdgcn_mfma_f32_32x32x16_bf16(b1, qr[d0], d0 == 0 ? negm : p1, 0, 0, 0); }
; template <bool FIXM> __device__ __forceinline__ void pv_psm(f32x16& o0, f32x16& o1, unsigned vb, bf16x8 pa0, bf16x8 pa1, bf16x8 pa2, bf16x8 pa3,
;                                        f32x16& p0, f32x16& p1, float& m_reg, f32x16& negm, float& alpha) {
;     { const s16x4 l0 = tr_read<v_rd_off(0, 0, 0)>(vb), h0 = tr_read<v_rd_off(0, 0, 1)>(vb), l1 = tr_read<v_rd_off(0, 1, 0)>(vb), h1 = tr_read<v_rd_off(0, 1, 1)>(vb);
;       const s16x4 l2 = tr_read<v_rd_off(0, 2, 0)>(vb), h2 = tr_read<v_rd_off(0, 2, 1)>(vb), l3 = tr_read<v_rd_off(0, 3, 0)>(vb), h3 = tr_read<v_rd_off(0, 3, 1)>(vb);
;       float pmax = 0.f; SBAR(); if (!FIXM) pmax = psm_max(p0, p1); else { _Pragma("unroll") for (int r = 0; r < 8; ++r) p0[r] = __builtin_amdgcn_exp2f(p0[r]); } SBAR();
;       asm volatile("s_waitcnt lgkmcnt(0)" ::: "memory"); SBAR();
;       o0 = __builtin_amdgcn_mfma_f32_32x32x16_bf16(ATT_PK(l0, h0), pa0, o0, 0, 0, 0);
;       o0 = __builtin_amdgcn_mfma_f32_32x32x16_bf16(ATT_PK(l1, h1), pa1, o0, 0, 0, 0);
	ds_read_b128 v[224:227], v223 offset:20480
	ds_read_b128 v[228:231], v223 offset:24576
	ds_read_b128 v[232:235], v252 offset:20480
	ds_read_b128 v[236:239], v252 offset:24576
	ds_read_b128 v[240:243], v253 offset:20480
	ds_read_b128 v[244:247], v253 offset:24576
	ds_read_b128 v[248:251], v2 offset:20480
	v_exp_f32_e32 v82, v82
	v_exp_f32_e32 v83, v83
	v_exp_f32_e32 v84, v84
	v_exp_f32_e32 v85, v85
	v_exp_f32_e32 v86, v86
	v_exp_f32_e32 v87, v87
	v_exp_f32_e32 v88, v88
	v_exp_f32_e32 v89, v89
	s_waitcnt lgkmcnt(6)
	v_mfma_f32_32x32x16_bf16 v[98:113], v[224:227], v[114:117], v[18:33]
	ds_read_b128 v[224:227], v2 offset:24576
	v_exp_f32_e32 v90, v90
	v_exp_f32_e32 v91, v91
	v_exp_f32_e32 v92, v92
	v_cvt_pk_bf16_f32 v156, v168, v169
	v_cvt_pk_bf16_f32 v157, v170, v171
	v_add_f32_e32 v164, v168, v169
	v_add_f32_e32 v164, v170, v164
	s_waitcnt lgkmcnt(6)
	v_mfma_f32_32x32x16_bf16 v[66:81], v[228:231], v[114:117], v[18:33]
	v_exp_f32_e32 v93, v93
	v_exp_f32_e32 v94, v94
	v_exp_f32_e32 v95, v95
	v_cvt_pk_bf16_f32 v158, v172, v173
	v_cvt_pk_bf16_f32 v159, v174, v175
	v_add_f32_e32 v164, v171, v164
	v_add_f32_e32 v164, v172, v164
	v_add_f32_e32 v164, v173, v164
	s_waitcnt lgkmcnt(5)
	v_mfma_f32_32x32x16_bf16 v[98:113], v[232:235], v[12:15], v[98:113]
	v_exp_f32_e32 v96, v96
	v_exp_f32_e32 v97, v97
	v_cvt_pk_bf16_f32 v160, v176, v177
	v_cvt_pk_bf16_f32 v161, v178, v179
	v_cvt_pk_bf16_f32 v162, v180, v181
	v_cvt_pk_bf16_f32 v163, v182, v183
	v_add_f32_e32 v164, v174, v164
	v_add_f32_e32 v164, v175, v164
	v_add_f32_e32 v164, v176, v164
	s_waitcnt lgkmcnt(4)
	v_mfma_f32_32x32x16_bf16 v[66:81], v[236:239], v[12:15], v[66:81]
	v_add_f32_e32 v164, v177, v164
	v_add_f32_e32 v164, v178, v164
	v_add_f32_e32 v164, v179, v164
	v_add_f32_e32 v164, v180, v164
	v_add_f32_e32 v164, v181, v164
	v_add_f32_e32 v164, v182, v164
	v_add_f32_e32 v164, v183, v164
	s_waitcnt lgkmcnt(3)
	v_mfma_f32_32x32x16_bf16 v[98:113], v[240:243], v[8:11], v[98:113]
	ds_read_b64_tr_b16 v[168:169], v213 offset:0
	ds_read_b64_tr_b16 v[170:171], v213 offset:1024
	ds_read_b64_tr_b16 v[172:173], v213 offset:2048
	ds_read_b64_tr_b16 v[174:175], v213 offset:3072
	v_add_f32_e32 v164, v82, v164
	v_add_f32_e32 v164, v83, v164
	v_add_f32_e32 v164, v84, v164
	v_add_f32_e32 v164, v85, v164
	s_waitcnt lgkmcnt(6)
	v_mfma_f32_32x32x16_bf16 v[66:81], v[244:247], v[8:11], v[66:81]
	ds_read_b64_tr_b16 v[176:177], v213 offset:4096
	ds_read_b64_tr_b16 v[178:179], v213 offset:5120
	ds_read_b64_tr_b16 v[180:181], v213 offset:6144
	ds_read_b64_tr_b16 v[182:183], v213 offset:7168
	v_add_f32_e32 v164, v86, v164
	v_add_f32_e32 v164, v87, v164
	v_add_f32_e32 v164, v88, v164
	v_add_f32_e32 v164, v89, v164
	s_waitcnt lgkmcnt(9)
	v_mfma_f32_32x32x16_bf16 v[98:113], v[248:251], v[4:7], v[98:113]
	v_add_f32_e32 v164, v90, v164
	v_add_f32_e32 v164, v91, v164
	v_add_f32_e32 v164, v92, v164
	v_add_f32_e32 v164, v93, v164
	s_waitcnt lgkmcnt(8)
	v_mfma_f32_32x32x16_bf16 v[66:81], v[224:227], v[4:7], v[66:81]
	ds_read_b64_tr_b16 v[224:225], v213 offset:512
	ds_read_b64_tr_b16 v[226:227], v213 offset:1536
	ds_read_b64_tr_b16 v[228:229], v213 offset:2560
	ds_read_b64_tr_b16 v[230:231], v213 offset:3584
	ds_read_b64_tr_b16 v[232:233], v213 offset:4608
	ds_read_b64_tr_b16 v[234:235], v213 offset:5632
	ds_read_b64_tr_b16 v[236:237], v213 offset:6656
	ds_read_b64_tr_b16 v[238:239], v213 offset:7680
	s_waitcnt lgkmcnt(8)
	v_mfma_f32_32x32x16_bf16 v[50:65], v[168:171], v[156:159], v[50:65]
	v_add_f32_e32 v164, v94, v164
	v_add_f32_e32 v164, v95, v164
	v_add_f32_e32 v164, v96, v164
	v_add_f32_e32 v164, v97, v164
	v_mfma_f32_32x32x16_bf16 v[50:65], v[172:175], v[160:163], v[50:65]
	v_cvt_pk_bf16_f32 v82, v82, v83
	v_cvt_pk_bf16_f32 v83, v84, v85
	v_cvt_pk_bf16_f32 v84, v86, v87
	v_cvt_pk_bf16_f32 v85, v88, v89
	v_cvt_pk_bf16_f32 v86, v90, v91
	v_cvt_pk_bf16_f32 v87, v92, v93
	v_cvt_pk_bf16_f32 v88, v94, v95
	v_cvt_pk_bf16_f32 v89, v96, v97
	v_mfma_f32_32x32x16_bf16 v[50:65], v[176:179], v[82:85], v[50:65]
	v_mfma_f32_32x32x16_bf16 v[50:65], v[180:183], v[86:89], v[50:65]
	s_cmp_ge_u32 s13, s30
	s_cbranch_scc1 .Lgqa_b_noload_1
	s_cmp_lt_u32 s13, s31
	s_cselect_b32 s9, 0, s31
	s_cselect_b32 s35, s12, s29
	s_lshl_b32 s9, s9, 6
	s_sub_i32 s9, s35, s9
	s_lshl_b32 s52, s9, 8
	v_add_u32_e32 v122, s52, v137
	global_load_dwordx4 v[118:121], v122, s[42:43]
	global_load_dwordx4 v[122:125], v122, s[44:45]
; #define SBAR() __builtin_amdgcn_sched_barrier(0)
; __device__ __forceinline__ void finishSM(f32x16& p0, f32x16& p1, float alpha, float& l_reg, bf16x8& pa0, bf16x8& pa1, bf16x8& pa2, bf16x8& pa3) {
; #pragma unroll
; template <bool FIXM> __device__ __forceinline__ void pv_psm(f32x16& o0, f32x16& o1, unsigned vb, bf16x8 pa0, bf16x8 pa1, bf16x8 pa2, bf16x8 pa3,
;                                        f32x16& p0, f32x16& p1, float& m_reg, f32x16& negm, float& alpha) {
;     { const s16x4 l0 = tr_read<v_rd_off(0, 0, 0)>(vb), h0 = tr_read<v_rd_off(0, 0, 1)>(vb), l1 = tr_read<v_rd_off(0, 1, 0)>(vb), h1 = tr_read<v_rd_off(0, 1, 1)>(vb);
;       const s16x4 l2 = tr_read<v_rd_off(0, 2, 0)>(vb), h2 = tr_read<v_rd_off(0, 2, 1)>(vb), l3 = tr_read<v_rd_off(0, 3, 0)>(vb), h3 = tr_read<v_rd_off(0, 3, 1)>(vb);
;       float pmax = 0.f; SBAR(); if (!FIXM) pmax = psm_max(p0, p1); else { _Pragma("unroll") for (int r = 0; r < 8; ++r) p0[r] = __builtin_amdgcn_exp2f(p0[r]); } SBAR();
;       asm volatile("s_waitcnt lgkmcnt(0)" ::: "memory"); SBAR();
;       o0 = __builtin_amdgcn_mfma_f32_32x32x16_bf16(ATT_PK(l0, h0), pa0, o0, 0, 0, 0);
;       o0 = __builtin_amdgcn_mfma_f32_32x32x16_bf16(ATT_PK(l1, h1), pa1, o0, 0, 0, 0);
;       o0 = __builtin_amdgcn_mfma_f32_32x32x16_bf16(ATT_PK(l2, h2), pa2, o0, 0, 0, 0);
;       o0 = __builtin_amdgcn_mfma_f32_32x32x16_bf16(ATT_PK(l3, h3), pa3, o0, 0, 0, 0);
;       SBAR();
;       const s16x4 m0 = tr_read<v_rd_off(1, 0, 0)>(vb), n0 = tr_read<v_rd_off(1, 0, 1)>(vb), m1 = tr_read<v_rd_off(1, 1, 0)>(vb), n1 = tr_read<v_rd_off(1, 1, 1)>(vb);
;       const s16x4 m2 = tr_read<v_rd_off(1, 2, 0)>(vb), n2 = tr_read<v_rd_off(1, 2, 1)>(vb), m3 = tr_read<v_rd_off(1, 3, 0)>(vb), n3 = tr_read<v_rd_off(1, 3, 1)>(vb);
;       SBAR(); if (!FIXM) psm_apply<false>(p0, p1, pmax, m_reg, negm, alpha); else { alpha = 1.f; _Pragma("unroll") for (int r = 8; r < 16; ++r) p0[r] = __builtin_amdgcn_exp2f(p0[r]); } SBAR();
;       asm volatile("s_waitcnt lgkmcnt(0)" ::: "memory"); SBAR();
;       o1 = __builtin_amdgcn_mfma_f32_32x32x16_bf16(ATT_PK(m0, n0), pa0, o1, 0, 0, 0);
;       o1 = __builtin_amdgcn_mfma_f32_32x32x16_bf16(ATT_PK(m1, n1), pa1, o1, 0, 0, 0);
;       o1 = __builtin_amdgcn_mfma_f32_32x32x16_bf16(ATT_PK(m2, n2), pa2, o1, 0, 0, 0);
;       o1 = __builtin_amdgcn_mfma_f32_32x32x16_bf16(ATT_PK(m3, n3), pa3, o1, 0, 0, 0); }
; }
.Lgqa_b_ld_done_1:
	s_waitcnt lgkmcnt(0)
	v_mfma_f32_32x32x16_bf16 v[34:49], v[224:227], v[156:159], v[34:49]
	s_waitcnt vmcnt(2)
	ds_write_b128 v187, v[130:133] offset:40960
	ds_write_b128 v214, v[126:129] offset:53248
	v_exp_f32_e32 v143, v98
	v_exp_f32_e32 v145, v99
	v_mfma_f32_32x32x16_bf16 v[34:49], v[228:231], v[160:163], v[34:49]
	v_exp_f32_e32 v141, v100
	v_exp_f32_e32 v144, v101
	v_exp_f32_e32 v139, v102
	v_exp_f32_e32 v142, v103
	v_mfma_f32_32x32x16_bf16 v[34:49], v[232:235], v[82:85], v[34:49]
	v_exp_f32_e32 v138, v104
	v_exp_f32_e32 v140, v105
	v_exp_f32_e32 v151, v106
	v_exp_f32_e32 v153, v107
	v_exp_f32_e32 v149, v108
	v_mfma_f32_32x32x16_bf16 v[34:49], v[236:239], v[86:89], v[34:49]
	v_exp_f32_e32 v152, v109
	v_exp_f32_e32 v147, v110
	v_exp_f32_e32 v150, v111
	v_exp_f32_e32 v146, v112
	v_exp_f32_e32 v148, v113
	v_add_f32_e32 v136, v136, v154
	v_add_f32_e32 v136, v136, v164
	s_add_i32 s13, s13, 2
	v_add_u32_e32 v137, 0x8000, v137
	s_cmp_lt_u32 s8, s0
	s_cbranch_scc0 .Lgqa_exit_1
	s_waitcnt lgkmcnt(0)
	s_barrier
	ds_read_b128 v[224:227], v223 offset:40960
	ds_read_b128 v[228:231], v223 offset:45056
	ds_read_b128 v[232:235], v252 offset:40960
	ds_read_b128 v[236:239], v252 offset:45056
	ds_read_b128 v[240:243], v253 offset:40960
	ds_read_b128 v[244:247], v253 offset:45056
	ds_read_b128 v[248:251], v2 offset:40960
	v_exp_f32_e32 v66, v66
	v_exp_f32_e32 v67, v67
	v_exp_f32_e32 v68, v68
	v_exp_f32_e32 v69, v69
	v_exp_f32_e32 v70, v70
	v_exp_f32_e32 v71, v71
	v_exp_f32_e32 v72, v72
	v_exp_f32_e32 v73, v73
	s_waitcnt lgkmcnt(6)
	v_mfma_f32_32x32x16_bf16 v[98:113], v[224:227], v[114:117], v[18:33]
	ds_read_b128 v[224:227], v2 offset:45056
	v_exp_f32_e32 v74, v74
	v_exp_f32_e32 v75, v75
	v_exp_f32_e32 v76, v76
	v_cvt_pk_bf16_f32 v156, v143, v145
	v_cvt_pk_bf16_f32 v157, v141, v144
	v_add_f32_e32 v164, v143, v145
	v_add_f32_e32 v164, v141, v164
	s_waitcnt lgkmcnt(6)
	v_mfma_f32_32x32x16_bf16 v[82:97], v[228:231], v[114:117], v[18:33]
	v_exp_f32_e32 v77, v77
	v_exp_f32_e32 v78, v78
	v_exp_f32_e32 v79, v79
	v_cvt_pk_bf16_f32 v158, v139, v142
	v_cvt_pk_bf16_f32 v159, v138, v140
	v_add_f32_e32 v164, v144, v164
	v_add_f32_e32 v164, v139, v164
	v_add_f32_e32 v164, v142, v164
	s_waitcnt lgkmcnt(5)
	v_mfma_f32_32x32x16_bf16 v[98:113], v[232:235], v[12:15], v[98:113]
	v_exp_f32_e32 v80, v80
	v_exp_f32_e32 v81, v81
	v_cvt_pk_bf16_f32 v160, v151, v153
	v_cvt_pk_bf16_f32 v161, v149, v152
	v_cvt_pk_bf16_f32 v162, v147, v150
	v_cvt_pk_bf16_f32 v163, v146, v148
	v_add_f32_e32 v164, v138, v164
	v_add_f32_e32 v164, v140, v164
	v_add_f32_e32 v164, v151, v164
	s_waitcnt lgkmcnt(4)
	v_mfma_f32_32x32x16_bf16 v[82:97], v[236:239], v[12:15], v[82:97]
	v_add_f32_e32 v164, v153, v164
	v_add_f32_e32 v164, v149, v164
	v_add_f32_e32 v164, v152, v164
	v_add_f32_e32 v164, v147, v164
	v_add_f32_e32 v164, v150, v164
	v_add_f32_e32 v164, v146, v164
	v_add_f32_e32 v164, v148, v164
	s_waitcnt lgkmcnt(3)
	v_mfma_f32_32x32x16_bf16 v[98:113], v[240:243], v[8:11], v[98:113]
	ds_read_b64_tr_b16 v[138:139], v213 offset:20480
	ds_read_b64_tr_b16 v[140:141], v213 offset:21504
	ds_read_b64_tr_b16 v[142:143], v213 offset:22528
	ds_read_b64_tr_b16 v[144:145], v213 offset:23552
	v_add_f32_e32 v164, v66, v164
	v_add_f32_e32 v164, v67, v164
	v_add_f32_e32 v164, v68, v164
	v_add_f32_e32 v164, v69, v164
	s_waitcnt lgkmcnt(6)
	v_mfma_f32_32x32x16_bf16 v[82:97], v[244:247], v[8:11], v[82:97]
	ds_read_b64_tr_b16 v[146:147], v213 offset:24576
	ds_read_b64_tr_b16 v[148:149], v213 offset:25600
	ds_read_b64_tr_b16 v[150:151], v213 offset:26624
	ds_read_b64_tr_b16 v[152:153], v213 offset:27648
	v_add_f32_e32 v164, v70, v164
	v_add_f32_e32 v164, v71, v164
	v_add_f32_e32 v164, v72, v164
	v_add_f32_e32 v164, v73, v164
	s_waitcnt lgkmcnt(9)
	v_mfma_f32_32x32x16_bf16 v[98:113], v[248:251], v[4:7], v[98:113]
	v_add_f32_e32 v164, v74, v164
	v_add_f32_e32 v164, v75, v164
	v_add_f32_e32 v164, v76, v164
	v_add_f32_e32 v164, v77, v164
	s_waitcnt lgkmcnt(8)
	v_mfma_f32_32x32x16_bf16 v[82:97], v[224:227], v[4:7], v[82:97]
	ds_read_b64_tr_b16 v[224:225], v213 offset:20992
	ds_read_b64_tr_b16 v[226:227], v213 offset:22016
	ds_read_b64_tr_b16 v[228:229], v213 offset:23040
	ds_read_b64_tr_b16 v[230:231], v213 offset:24064
	ds_read_b64_tr_b16 v[232:233], v213 offset:25088
	ds_read_b64_tr_b16 v[234:235], v213 offset:26112
	ds_read_b64_tr_b16 v[236:237], v213 offset:27136
	ds_read_b64_tr_b16 v[238:239], v213 offset:28160
	s_waitcnt lgkmcnt(8)
	v_mfma_f32_32x32x16_bf16 v[50:65], v[138:141], v[156:159], v[50:65]
	v_add_f32_e32 v164, v78, v164
	v_add_f32_e32 v164, v79, v164
	v_add_f32_e32 v164, v80, v164
	v_add_f32_e32 v154, v81, v164
	v_mfma_f32_32x32x16_bf16 v[50:65], v[142:145], v[160:163], v[50:65]
	v_cvt_pk_bf16_f32 v66, v66, v67
	v_cvt_pk_bf16_f32 v67, v68, v69
	v_cvt_pk_bf16_f32 v68, v70, v71
	v_cvt_pk_bf16_f32 v69, v72, v73
	v_cvt_pk_bf16_f32 v70, v74, v75
	v_cvt_pk_bf16_f32 v71, v76, v77
	v_cvt_pk_bf16_f32 v72, v78, v79
	v_cvt_pk_bf16_f32 v73, v80, v81
	v_mfma_f32_32x32x16_bf16 v[50:65], v[146:149], v[66:69], v[50:65]
	s_add_i32 s8, s13, -1
	s_cmp_lt_u32 s8, s31
	s_cselect_b32 s9, 0, s31
	s_cselect_b32 s35, s12, s29
	s_lshl_b32 s9, s9, 6
	s_sub_i32 s9, s35, s9
	s_lshl_b32 s52, s9, 8
	s_add_i32 s52, s52, -16384
	v_mfma_f32_32x32x16_bf16 v[50:65], v[150:153], v[70:73], v[50:65]
	v_add_u32_e32 v126, s52, v137
	global_load_dwordx4 v[130:133], v126, s[42:43]
	global_load_dwordx4 v[126:129], v126, s[44:45]
	s_waitcnt lgkmcnt(0)
	v_mfma_f32_32x32x16_bf16 v[34:49], v[224:227], v[156:159], v[34:49]
	s_waitcnt vmcnt(2)
	ds_write_b128 v187, v[118:121] offset:0
	ds_write_b128 v214, v[122:125] offset:12288
	v_exp_f32_e32 v168, v98
	v_exp_f32_e32 v169, v99
	v_mfma_f32_32x32x16_bf16 v[34:49], v[228:231], v[160:163], v[34:49]
	v_exp_f32_e32 v170, v100
	v_exp_f32_e32 v171, v101
	v_exp_f32_e32 v172, v102
	v_exp_f32_e32 v173, v103
	v_mfma_f32_32x32x16_bf16 v[34:49], v[232:235], v[66:69], v[34:49]
	v_exp_f32_e32 v174, v104
	v_exp_f32_e32 v175, v105
	v_exp_f32_e32 v176, v106
	v_exp_f32_e32 v177, v107
	v_exp_f32_e32 v178, v108
	v_mfma_f32_32x32x16_bf16 v[34:49], v[236:239], v[70:73], v[34:49]
	v_exp_f32_e32 v179, v109
	v_exp_f32_e32 v180, v110
	v_exp_f32_e32 v181, v111
	v_exp_f32_e32 v182, v112
	v_exp_f32_e32 v183, v113
	s_waitcnt lgkmcnt(0)
	s_barrier
; #define SBAR() __builtin_amdgcn_sched_barrier(0)
; #define ATT_PKN(P, BASE, OUT) do { u32x4 w = {cvt_pk_bf16(P[BASE + 0], P[BASE + 1]), cvt_pk_bf16(P[BASE + 2], P[BASE + 3]), cvt_pk_bf16(P[BASE + 4], P[BASE + 5]), cvt_pk_bf16(P[BASE + 6], P[BASE + 7])}; \
;     OUT = __builtin_bit_cast(bf16x8, w); } while (0)
; #define SLOAD(i, j) do { const int _row = KROW(j); skn[i] = *(const bf16x8*)(Knp + (size_t)(_row + sr) * ldk + c8 * 8); sv[i] = *(const bf16x8*)(Vp + (size_t)(_row + sr) * ldv + c8 * 8); \
;         if (krw) skr[i] = *(const bf16x8*)(Krp + (size_t)(_row + sr2) * 32 + c4 * 8); } while (0)
; __device__ __forceinline__ void finishSM(f32x16& p0, f32x16& p1, float alpha, float& l_reg, bf16x8& pa0, bf16x8& pa1, bf16x8& pa2, bf16x8& pa3) {
; #pragma unroll
;     for (int r = 0; r < 16; ++r) p1[r] = EXP_PROBE ? fmaf(p1[r], 0.001f, 1.f) : __builtin_amdgcn_exp2f(p1[r]);
;     float ps = 0.f;
; #pragma unroll
;     for (int r = 0; r < 16; ++r) ps += p0[r];
; #pragma unroll
;     for (int r = 0; r < 16; ++r) ps += p1[r];
;     { auto rr = __builtin_amdgcn_permlane32_swap(__float_as_uint(ps), __float_as_uint(ps), false, false);
;       ps = __uint_as_float(rr[0]) + __uint_as_float(rr[1]); }
;     l_reg = l_reg * alpha + ps;
;     ATT_PKN(p0, 0, pa0); ATT_PKN(p0, 8, pa1); ATT_PKN(p1, 0, pa2); ATT_PKN(p1, 8, pa3);
; }
; template <int DQK, bool FIXM> ...
;     ...
;     for (int j = 1; j + 1 < NT; j += 2) {
;         if (!NOBAR_PROBE) __syncthreads();
;         SBAR(); qkt<DQK>(pB0, pB1, lds + bK, qr, r32, hi, negm);
;         finishSM(pA0, pA1, alA, l_reg, pa0, pa1, pa2, pa3); SBAR();
;         SLOAD(1, j + 2); SBAR();
;         if constexpr (FIXM) pv_psm<true>(o0, o1, vb0 + bV, pa0, pa1, pa2, pa3, pB0, pB1, m_reg, negm, alB); else { PVO(bV); partialSM<false>(pB0, pB1, m_reg, negm, alB); }
;         SWAIT(); SWRITEO(bW, 0);
;         if (!FIXM) RESC(alB); ROT();
;         if (!NOBAR_PROBE) __syncthreads();
;         SBAR(); qkt<DQK>(pA0, pA1, lds + bK, qr, r32, hi, negm);
;         finishSM(pB0, pB1, alB, l_reg, pa0, pa1, pa2, pa3); SBAR();
;         if (j + 3 < NT) SLOAD(0, j + 3); SBAR();
;         if constexpr (FIXM) pv_psm<true>(o0, o1, vb0 + bV, pa0, pa1, pa2, pa3, pA0, pA1, m_reg, negm, alA); else { PVO(bV); partialSM<false>(pA0, pA1, m_reg, negm, alA); }
;         SWAIT(); SWRITEO(bW, 1);
;         if (!FIXM) RESC(alA); ROT();
;     }
	ds_read_b128 v[224:227], v223 offset:0
	ds_read_b128 v[228:231], v223 offset:4096
	ds_read_b128 v[232:235], v252 offset:0
	ds_read_b128 v[236:239], v252 offset:4096
	ds_read_b128 v[240:243], v253 offset:0
	ds_read_b128 v[244:247], v253 offset:4096
	ds_read_b128 v[248:251], v2 offset:0
	v_exp_f32_e32 v82, v82
	v_exp_f32_e32 v83, v83
	v_exp_f32_e32 v84, v84
	v_exp_f32_e32 v85, v85
	v_exp_f32_e32 v86, v86
	v_exp_f32_e32 v87, v87
	v_exp_f32_e32 v88, v88
	v_exp_f32_e32 v89, v89
	s_waitcnt lgkmcnt(6)
	v_mfma_f32_32x32x16_bf16 v[98:113], v[224:227], v[114:117], v[18:33]
	ds_read_b128 v[224:227], v2 offset:4096
	v_exp_f32_e32 v90, v90
	v_exp_f32_e32 v91, v91
	v_exp_f32_e32 v92, v92
	v_cvt_pk_bf16_f32 v156, v168, v169
	v_cvt_pk_bf16_f32 v157, v170, v171
	v_add_f32_e32 v164, v168, v169
	v_add_f32_e32 v164, v170, v164
	s_waitcnt lgkmcnt(6)
	v_mfma_f32_32x32x16_bf16 v[66:81], v[228:231], v[114:117], v[18:33]
	v_exp_f32_e32 v93, v93
	v_exp_f32_e32 v94, v94
	v_exp_f32_e32 v95, v95
	v_cvt_pk_bf16_f32 v158, v172, v173
	v_cvt_pk_bf16_f32 v159, v174, v175
	v_add_f32_e32 v164, v171, v164
	v_add_f32_e32 v164, v172, v164
	v_add_f32_e32 v164, v173, v164
	s_waitcnt lgkmcnt(5)
	v_mfma_f32_32x32x16_bf16 v[98:113], v[232:235], v[12:15], v[98:113]
	v_exp_f32_e32 v96, v96
	v_exp_f32_e32 v97, v97
	v_cvt_pk_bf16_f32 v160, v176, v177
	v_cvt_pk_bf16_f32 v161, v178, v179
	v_cvt_pk_bf16_f32 v162, v180, v181
	v_cvt_pk_bf16_f32 v163, v182, v183
	v_add_f32_e32 v164, v174, v164
	v_add_f32_e32 v164, v175, v164
	v_add_f32_e32 v164, v176, v164
	s_waitcnt lgkmcnt(4)
	v_mfma_f32_32x32x16_bf16 v[66:81], v[236:239], v[12:15], v[66:81]
	v_add_f32_e32 v164, v177, v164
	v_add_f32_e32 v164, v178, v164
	v_add_f32_e32 v164, v179, v164
	v_add_f32_e32 v164, v180, v164
	v_add_f32_e32 v164, v181, v164
	v_add_f32_e32 v164, v182, v164
	v_add_f32_e32 v164, v183, v164
	s_waitcnt lgkmcnt(3)
	v_mfma_f32_32x32x16_bf16 v[98:113], v[240:243], v[8:11], v[98:113]
	ds_read_b64_tr_b16 v[168:169], v213 offset:40960
	ds_read_b64_tr_b16 v[170:171], v213 offset:41984
	ds_read_b64_tr_b16 v[172:173], v213 offset:43008
	ds_read_b64_tr_b16 v[174:175], v213 offset:44032
	v_add_f32_e32 v164, v82, v164
	v_add_f32_e32 v164, v83, v164
	v_add_f32_e32 v164, v84, v164
	v_add_f32_e32 v164, v85, v164
	s_waitcnt lgkmcnt(6)
	v_mfma_f32_32x32x16_bf16 v[66:81], v[244:247], v[8:11], v[66:81]
	ds_read_b64_tr_b16 v[176:177], v213 offset:45056
	ds_read_b64_tr_b16 v[178:179], v213 offset:46080
	ds_read_b64_tr_b16 v[180:181], v213 offset:47104
	ds_read_b64_tr_b16 v[182:183], v213 offset:48128
	v_add_f32_e32 v164, v86, v164
	v_add_f32_e32 v164, v87, v164
	v_add_f32_e32 v164, v88, v164
	v_add_f32_e32 v164, v89, v164
	s_waitcnt lgkmcnt(9)
	v_mfma_f32_32x32x16_bf16 v[98:113], v[248:251], v[4:7], v[98:113]
	v_add_f32_e32 v164, v90, v164
	v_add_f32_e32 v164, v91, v164
	v_add_f32_e32 v164, v92, v164
	v_add_f32_e32 v164, v93, v164
	s_waitcnt lgkmcnt(8)
	v_mfma_f32_32x32x16_bf16 v[66:81], v[224:227], v[4:7], v[66:81]
	ds_read_b64_tr_b16 v[224:225], v213 offset:41472
	ds_read_b64_tr_b16 v[226:227], v213 offset:42496
	ds_read_b64_tr_b16 v[228:229], v213 offset:43520
	ds_read_b64_tr_b16 v[230:231], v213 offset:44544
	ds_read_b64_tr_b16 v[232:233], v213 offset:45568
	ds_read_b64_tr_b16 v[234:235], v213 offset:46592
	ds_read_b64_tr_b16 v[236:237], v213 offset:47616
	ds_read_b64_tr_b16 v[238:239], v213 offset:48640
	s_waitcnt lgkmcnt(8)
	v_mfma_f32_32x32x16_bf16 v[50:65], v[168:171], v[156:159], v[50:65]
	v_add_f32_e32 v164, v94, v164
	v_add_f32_e32 v164, v95, v164
	v_add_f32_e32 v164, v96, v164
	v_add_f32_e32 v164, v97, v164
	v_mfma_f32_32x32x16_bf16 v[50:65], v[172:175], v[160:163], v[50:65]
	v_cvt_pk_bf16_f32 v82, v82, v83
	v_cvt_pk_bf16_f32 v83, v84, v85
	v_cvt_pk_bf16_f32 v84, v86, v87
	v_cvt_pk_bf16_f32 v85, v88, v89
	v_cvt_pk_bf16_f32 v86, v90, v91
	v_cvt_pk_bf16_f32 v87, v92, v93
	v_cvt_pk_bf16_f32 v88, v94, v95
	v_cvt_pk_bf16_f32 v89, v96, v97
	v_mfma_f32_32x32x16_bf16 v[50:65], v[176:179], v[82:85], v[50:65]
	v_mfma_f32_32x32x16_bf16 v[50:65], v[180:183], v[86:89], v[50:65]
	s_cmp_ge_u32 s13, s30
	s_cbranch_scc1 .Lgqa_b_noload_2
	s_cmp_lt_u32 s13, s31
	s_cselect_b32 s9, 0, s31
	s_cselect_b32 s35, s12, s29
	s_lshl_b32 s9, s9, 6
	s_sub_i32 s9, s35, s9
	s_lshl_b32 s52, s9, 8
	v_add_u32_e32 v122, s52, v137
	global_load_dwordx4 v[118:121], v122, s[42:43]
	global_load_dwordx4 v[122:125], v122, s[44:45]
.Lgqa_b_ld_done_2:
	s_waitcnt lgkmcnt(0)
	v_mfma_f32_32x32x16_bf16 v[34:49], v[224:227], v[156:159], v[34:49]
	s_waitcnt vmcnt(2)
	ds_write_b128 v187, v[130:133] offset:20480
	ds_write_b128 v214, v[126:129] offset:32768
	v_exp_f32_e32 v143, v98
	v_exp_f32_e32 v145, v99
	v_mfma_f32_32x32x16_bf16 v[34:49], v[228:231], v[160:163], v[34:49]
	v_exp_f32_e32 v141, v100
	v_exp_f32_e32 v144, v101
	v_exp_f32_e32 v139, v102
	v_exp_f32_e32 v142, v103
	v_mfma_f32_32x32x16_bf16 v[34:49], v[232:235], v[82:85], v[34:49]
	v_exp_f32_e32 v138, v104
	v_exp_f32_e32 v140, v105
	v_exp_f32_e32 v151, v106
	v_exp_f32_e32 v153, v107
	v_exp_f32_e32 v149, v108
	v_mfma_f32_32x32x16_bf16 v[34:49], v[236:239], v[86:89], v[34:49]
	v_exp_f32_e32 v152, v109
	v_exp_f32_e32 v147, v110
	v_exp_f32_e32 v150, v111
	v_exp_f32_e32 v146, v112
	v_exp_f32_e32 v148, v113
	v_add_f32_e32 v136, v136, v154
	v_add_f32_e32 v136, v136, v164
	s_add_i32 s13, s13, 2
	v_add_u32_e32 v137, 0x8000, v137
	s_cmp_lt_u32 s8, s0
	s_cbranch_scc1 .LBB0_497
.Lgqa_exit_2:
	s_movk_i32 s11, 20480
	s_mov_b32 s10, 0
	s_mov_b32 s1, 40960
	s_mov_b32 s9, s11
	v_add_u32_e32 v2, s11, v213
	v_mov_b32_e32 v252, v136
	s_nop 1
	v_permlane32_swap_b32_e32 v136, v252
	v_add_f32_e32 v136, v136, v252
	s_branch .LBB0_501
.Lgqa_exit_1:
	s_mov_b32 s11, 40960
	s_mov_b32 s10, 20480
	s_mov_b32 s1, 0
	s_mov_b32 s9, s11
	v_add_u32_e32 v2, s11, v213
	v_mov_b32_e32 v252, v136
	s_nop 1
	v_permlane32_swap_b32_e32 v136, v252
	v_add_f32_e32 v136, v136, v252
	s_branch .LBB0_501
.Lgqa_exit_0:
	s_movk_i32 s11, 0
	s_mov_b32 s10, 40960
	s_mov_b32 s1, 20480
	s_mov_b32 s9, s11
	v_add_u32_e32 v2, s11, v213
	v_mov_b32_e32 v252, v136
	s_nop 1
	v_permlane32_swap_b32_e32 v136, v252
	v_add_f32_e32 v136, v136, v252
	s_branch .LBB0_501
